# combine loop: the loads that do not depend on the routing positions (residual row, modulation vectors) of chunks 1..7 issued one round trip earlier, together with the position loads
# baseline (speedup 1.0000x reference)
.LBB0_2785:
	s_ashr_i32 s7, s6, 31
	s_lshl_b64 s[10:11], s[6:7], 2
	s_add_u32 s20, s14, s10
	s_addc_u32 s21, s15, s11
	global_load_dwordx2 v[10:11], v[4:5], off
	global_load_dwordx2 v[12:13], v1, s[20:21]
	s_add_i32 s22, s6, 1
	s_ashr_i32 s23, s22, 31
	s_add_u32 s10, s16, s10
	s_addc_u32 s11, s17, s11
	global_load_dword v0, v1, s[10:11]
	s_lshl_b64 s[20:21], s[22:23], 2
	s_add_u32 s10, s16, s20
	s_addc_u32 s11, s17, s21
	s_ashr_i32 s1, s0, 11
	s_mul_hi_i32 s3, s1, 0xc000
	s_mul_i32 s1, s1, 0xc000
	global_load_dword v8, v1, s[10:11]
	s_add_u32 s10, s12, s1
	s_addc_u32 s11, s13, s3
	global_load_dwordx4 v[18:21], v9, s[10:11]
	global_load_dwordx2 v[34:35], v[4:5], off offset:512
	global_load_dwordx4 v[40:43], v9, s[10:11] offset:1024
	global_load_dwordx2 v[44:45], v[4:5], off offset:1024
	global_load_dwordx4 v[50:53], v9, s[10:11] offset:2048
	global_load_dwordx2 v[54:55], v[4:5], off offset:1536
	global_load_dwordx4 v[60:63], v9, s[10:11] offset:3072
	global_load_dwordx2 v[64:65], v[4:5], off offset:2048
	global_load_dwordx4 v[70:73], v14, s[10:11]
	global_load_dwordx2 v[74:75], v[4:5], off offset:2560
	global_load_dwordx4 v[80:83], v15, s[10:11]
	global_load_dwordx2 v[84:85], v[4:5], off offset:3072
	global_load_dwordx4 v[90:93], v16, s[10:11]
	global_load_dwordx2 v[94:95], v[4:5], off offset:3584
	global_load_dwordx4 v[100:103], v17, s[10:11]
	s_add_i32 s0, s0, s2
	s_add_i32 s6, s6, s18
	s_cmp_lt_i32 s0, 0x8000
	s_waitcnt vmcnt(18)
	v_lshlrev_b32_e32 v22, 16, v10
	v_and_b32_e32 v23, 0xffff0000, v10
	v_lshlrev_b32_e32 v24, 16, v11
	v_and_b32_e32 v25, 0xffff0000, v11
	s_waitcnt vmcnt(17)
	v_ashrrev_i32_e32 v11, 31, v12
	v_mov_b32_e32 v10, v12
	v_ashrrev_i32_e32 v27, 31, v13
	v_mov_b32_e32 v26, v13
	v_lshlrev_b64 v[10:11], 12, v[10:11]
	v_lshlrev_b64 v[12:13], 12, v[26:27]
	v_lshl_add_u64 v[10:11], v[2:3], 0, v[10:11]
	v_lshl_add_u64 v[12:13], v[2:3], 0, v[12:13]
	global_load_dwordx2 v[26:27], v[10:11], off
	global_load_dwordx2 v[28:29], v[12:13], off
	global_load_dwordx2 v[36:37], v[10:11], off offset:512
	global_load_dwordx2 v[38:39], v[12:13], off offset:512
	global_load_dwordx2 v[46:47], v[10:11], off offset:1024
	global_load_dwordx2 v[48:49], v[12:13], off offset:1024
	global_load_dwordx2 v[56:57], v[10:11], off offset:1536
	global_load_dwordx2 v[58:59], v[12:13], off offset:1536
	global_load_dwordx2 v[66:67], v[10:11], off offset:2048
	global_load_dwordx2 v[68:69], v[12:13], off offset:2048
	global_load_dwordx2 v[76:77], v[10:11], off offset:2560
	global_load_dwordx2 v[78:79], v[12:13], off offset:2560
	global_load_dwordx2 v[86:87], v[10:11], off offset:3072
	global_load_dwordx2 v[88:89], v[12:13], off offset:3072
	global_load_dwordx2 v[96:97], v[10:11], off offset:3584
	global_load_dwordx2 v[98:99], v[12:13], off offset:3584
	s_waitcnt vmcnt(15)
	v_lshlrev_b32_e32 v30, 16, v26
	s_waitcnt vmcnt(14)
	v_lshlrev_b32_e32 v32, 16, v28
	v_and_b32_e32 v33, 0xffff0000, v28
	v_lshlrev_b32_e32 v28, 16, v29
	v_and_b32_e32 v29, 0xffff0000, v29
	v_and_b32_e32 v31, 0xffff0000, v26
	v_lshlrev_b32_e32 v26, 16, v27
	v_and_b32_e32 v27, 0xffff0000, v27
	v_pk_mul_f32 v[32:33], v[8:9], v[32:33] op_sel_hi:[0,1]
	v_pk_mul_f32 v[28:29], v[8:9], v[28:29] op_sel_hi:[0,1]
	v_pk_fma_f32 v[30:31], v[0:1], v[30:31], v[32:33] op_sel_hi:[0,1,1]
	v_pk_fma_f32 v[26:27], v[0:1], v[26:27], v[28:29] op_sel_hi:[0,1,1]
	v_pk_fma_f32 v[18:19], v[18:19], v[30:31], v[22:23]
	v_pk_fma_f32 v[20:21], v[20:21], v[26:27], v[24:25]
	global_store_dwordx4 v[6:7], v[18:21], off offset:-4096
	s_nop 0
	s_nop 0
	s_nop 0
	s_nop 0
	s_nop 0
	s_waitcnt vmcnt(13)
	v_mov_b32_e32 v22, v34
	v_mov_b32_e32 v23, v35
	v_mov_b32_e32 v24, v36
	v_mov_b32_e32 v25, v37
	v_mov_b32_e32 v26, v38
	v_mov_b32_e32 v27, v39
	v_mov_b32_e32 v18, v40
	v_mov_b32_e32 v19, v41
	v_mov_b32_e32 v20, v42
	v_mov_b32_e32 v21, v43
	v_lshlrev_b32_e32 v28, 16, v22
	s_nop 0
	v_lshlrev_b32_e32 v30, 16, v24
	s_nop 0
	v_lshlrev_b32_e32 v32, 16, v26
	v_and_b32_e32 v33, 0xffff0000, v26
	v_lshlrev_b32_e32 v26, 16, v27
	v_and_b32_e32 v27, 0xffff0000, v27
	v_and_b32_e32 v31, 0xffff0000, v24
	v_lshlrev_b32_e32 v24, 16, v25
	v_and_b32_e32 v25, 0xffff0000, v25
	v_pk_mul_f32 v[32:33], v[8:9], v[32:33] op_sel_hi:[0,1]
	v_pk_mul_f32 v[26:27], v[8:9], v[26:27] op_sel_hi:[0,1]
	v_and_b32_e32 v29, 0xffff0000, v22
	v_lshlrev_b32_e32 v22, 16, v23
	v_and_b32_e32 v23, 0xffff0000, v23
	v_pk_fma_f32 v[30:31], v[0:1], v[30:31], v[32:33] op_sel_hi:[0,1,1]
	v_pk_fma_f32 v[24:25], v[0:1], v[24:25], v[26:27] op_sel_hi:[0,1,1]
	s_nop 0
	v_pk_fma_f32 v[18:19], v[18:19], v[30:31], v[28:29]
	v_pk_fma_f32 v[20:21], v[20:21], v[24:25], v[22:23]
	global_store_dwordx4 v[6:7], v[18:21], off offset:-3072
	s_nop 0
	s_nop 0
	s_nop 0
	s_nop 0
	s_nop 0
	s_waitcnt vmcnt(12)
	v_mov_b32_e32 v22, v44
	v_mov_b32_e32 v23, v45
	v_mov_b32_e32 v24, v46
	v_mov_b32_e32 v25, v47
	v_mov_b32_e32 v26, v48
	v_mov_b32_e32 v27, v49
	v_mov_b32_e32 v18, v50
	v_mov_b32_e32 v19, v51
	v_mov_b32_e32 v20, v52
	v_mov_b32_e32 v21, v53
	v_lshlrev_b32_e32 v28, 16, v22
	s_nop 0
	v_lshlrev_b32_e32 v30, 16, v24
	s_nop 0
	v_lshlrev_b32_e32 v32, 16, v26
	v_and_b32_e32 v33, 0xffff0000, v26
	v_lshlrev_b32_e32 v26, 16, v27
	v_and_b32_e32 v27, 0xffff0000, v27
	v_and_b32_e32 v31, 0xffff0000, v24
	v_lshlrev_b32_e32 v24, 16, v25
	v_and_b32_e32 v25, 0xffff0000, v25
	v_pk_mul_f32 v[32:33], v[8:9], v[32:33] op_sel_hi:[0,1]
	v_pk_mul_f32 v[26:27], v[8:9], v[26:27] op_sel_hi:[0,1]
	v_and_b32_e32 v29, 0xffff0000, v22
	v_lshlrev_b32_e32 v22, 16, v23
	v_and_b32_e32 v23, 0xffff0000, v23
	v_pk_fma_f32 v[30:31], v[0:1], v[30:31], v[32:33] op_sel_hi:[0,1,1]
	v_pk_fma_f32 v[24:25], v[0:1], v[24:25], v[26:27] op_sel_hi:[0,1,1]
	s_nop 0
	v_pk_fma_f32 v[18:19], v[18:19], v[30:31], v[28:29]
	v_pk_fma_f32 v[20:21], v[20:21], v[24:25], v[22:23]
	global_store_dwordx4 v[6:7], v[18:21], off offset:-2048
	s_nop 0
	s_nop 0
	s_nop 0
	s_nop 0
	s_nop 0
	s_waitcnt vmcnt(11)
	v_mov_b32_e32 v22, v54
	v_mov_b32_e32 v23, v55
	v_mov_b32_e32 v24, v56
	v_mov_b32_e32 v25, v57
	v_mov_b32_e32 v26, v58
	v_mov_b32_e32 v27, v59
	v_mov_b32_e32 v18, v60
	v_mov_b32_e32 v19, v61
	v_mov_b32_e32 v20, v62
	v_mov_b32_e32 v21, v63
	v_lshlrev_b32_e32 v28, 16, v22
	s_nop 0
	v_lshlrev_b32_e32 v30, 16, v24
	s_nop 0
	v_lshlrev_b32_e32 v32, 16, v26
	v_and_b32_e32 v33, 0xffff0000, v26
	v_lshlrev_b32_e32 v26, 16, v27
	v_and_b32_e32 v27, 0xffff0000, v27
	v_and_b32_e32 v31, 0xffff0000, v24
	v_lshlrev_b32_e32 v24, 16, v25
	v_and_b32_e32 v25, 0xffff0000, v25
	v_pk_mul_f32 v[32:33], v[8:9], v[32:33] op_sel_hi:[0,1]
	v_pk_mul_f32 v[26:27], v[8:9], v[26:27] op_sel_hi:[0,1]
	v_and_b32_e32 v29, 0xffff0000, v22
	v_lshlrev_b32_e32 v22, 16, v23
	v_and_b32_e32 v23, 0xffff0000, v23
	v_pk_fma_f32 v[30:31], v[0:1], v[30:31], v[32:33] op_sel_hi:[0,1,1]
	v_pk_fma_f32 v[24:25], v[0:1], v[24:25], v[26:27] op_sel_hi:[0,1,1]
	s_nop 0
	v_pk_fma_f32 v[18:19], v[18:19], v[30:31], v[28:29]
	v_pk_fma_f32 v[20:21], v[20:21], v[24:25], v[22:23]
	global_store_dwordx4 v[6:7], v[18:21], off offset:-1024
	s_nop 0
	s_nop 0
	s_nop 0
	s_nop 0
	s_nop 0
	s_waitcnt vmcnt(10)
	v_mov_b32_e32 v22, v64
	v_mov_b32_e32 v23, v65
	v_mov_b32_e32 v24, v66
	v_mov_b32_e32 v25, v67
	v_mov_b32_e32 v26, v68
	v_mov_b32_e32 v27, v69
	v_mov_b32_e32 v18, v70
	v_mov_b32_e32 v19, v71
	v_mov_b32_e32 v20, v72
	v_mov_b32_e32 v21, v73
	v_lshlrev_b32_e32 v28, 16, v22
	s_nop 0
	v_lshlrev_b32_e32 v30, 16, v24
	s_nop 0
	v_lshlrev_b32_e32 v32, 16, v26
	v_and_b32_e32 v33, 0xffff0000, v26
	v_lshlrev_b32_e32 v26, 16, v27
	v_and_b32_e32 v27, 0xffff0000, v27
	v_and_b32_e32 v31, 0xffff0000, v24
	v_lshlrev_b32_e32 v24, 16, v25
	v_and_b32_e32 v25, 0xffff0000, v25
	v_pk_mul_f32 v[32:33], v[8:9], v[32:33] op_sel_hi:[0,1]
	v_pk_mul_f32 v[26:27], v[8:9], v[26:27] op_sel_hi:[0,1]
	v_and_b32_e32 v29, 0xffff0000, v22
	v_lshlrev_b32_e32 v22, 16, v23
	v_and_b32_e32 v23, 0xffff0000, v23
	v_pk_fma_f32 v[30:31], v[0:1], v[30:31], v[32:33] op_sel_hi:[0,1,1]
	v_pk_fma_f32 v[24:25], v[0:1], v[24:25], v[26:27] op_sel_hi:[0,1,1]
	s_nop 0
	v_pk_fma_f32 v[18:19], v[18:19], v[30:31], v[28:29]
	v_pk_fma_f32 v[20:21], v[20:21], v[24:25], v[22:23]
	global_store_dwordx4 v[6:7], v[18:21], off
	s_nop 0
	s_nop 0
	s_nop 0
	s_nop 0
	s_nop 0
	s_waitcnt vmcnt(9)
	v_mov_b32_e32 v22, v74
	v_mov_b32_e32 v23, v75
	v_mov_b32_e32 v24, v76
	v_mov_b32_e32 v25, v77
	v_mov_b32_e32 v26, v78
	v_mov_b32_e32 v27, v79
	v_mov_b32_e32 v18, v80
	v_mov_b32_e32 v19, v81
	v_mov_b32_e32 v20, v82
	v_mov_b32_e32 v21, v83
	v_lshlrev_b32_e32 v28, 16, v22
	s_nop 0
	v_lshlrev_b32_e32 v30, 16, v24
	s_nop 0
	v_lshlrev_b32_e32 v32, 16, v26
	v_and_b32_e32 v33, 0xffff0000, v26
	v_lshlrev_b32_e32 v26, 16, v27
	v_and_b32_e32 v27, 0xffff0000, v27
	v_and_b32_e32 v31, 0xffff0000, v24
	v_lshlrev_b32_e32 v24, 16, v25
	v_and_b32_e32 v25, 0xffff0000, v25
	v_pk_mul_f32 v[32:33], v[8:9], v[32:33] op_sel_hi:[0,1]
	v_pk_mul_f32 v[26:27], v[8:9], v[26:27] op_sel_hi:[0,1]
	v_and_b32_e32 v29, 0xffff0000, v22
	v_lshlrev_b32_e32 v22, 16, v23
	v_and_b32_e32 v23, 0xffff0000, v23
	v_pk_fma_f32 v[30:31], v[0:1], v[30:31], v[32:33] op_sel_hi:[0,1,1]
	v_pk_fma_f32 v[24:25], v[0:1], v[24:25], v[26:27] op_sel_hi:[0,1,1]
	s_nop 0
	v_pk_fma_f32 v[18:19], v[18:19], v[30:31], v[28:29]
	v_pk_fma_f32 v[20:21], v[20:21], v[24:25], v[22:23]
	global_store_dwordx4 v[6:7], v[18:21], off offset:1024
	s_nop 0
	s_nop 0
	s_nop 0
	s_nop 0
	s_nop 0
	s_waitcnt vmcnt(8)
	v_mov_b32_e32 v22, v84
	v_mov_b32_e32 v23, v85
	v_mov_b32_e32 v24, v86
	v_mov_b32_e32 v25, v87
	v_mov_b32_e32 v26, v88
	v_mov_b32_e32 v27, v89
	v_mov_b32_e32 v18, v90
	v_mov_b32_e32 v19, v91
	v_mov_b32_e32 v20, v92
	v_mov_b32_e32 v21, v93
	v_lshlrev_b32_e32 v28, 16, v22
	s_nop 0
	v_lshlrev_b32_e32 v30, 16, v24
	s_nop 0
	v_lshlrev_b32_e32 v32, 16, v26
	v_and_b32_e32 v33, 0xffff0000, v26
	v_lshlrev_b32_e32 v26, 16, v27
	v_and_b32_e32 v27, 0xffff0000, v27
	v_and_b32_e32 v31, 0xffff0000, v24
	v_lshlrev_b32_e32 v24, 16, v25
	v_and_b32_e32 v25, 0xffff0000, v25
	v_pk_mul_f32 v[32:33], v[8:9], v[32:33] op_sel_hi:[0,1]
	v_pk_mul_f32 v[26:27], v[8:9], v[26:27] op_sel_hi:[0,1]
	v_and_b32_e32 v29, 0xffff0000, v22
	v_lshlrev_b32_e32 v22, 16, v23
	v_and_b32_e32 v23, 0xffff0000, v23
	v_pk_fma_f32 v[30:31], v[0:1], v[30:31], v[32:33] op_sel_hi:[0,1,1]
	v_pk_fma_f32 v[24:25], v[0:1], v[24:25], v[26:27] op_sel_hi:[0,1,1]
	s_nop 0
	v_pk_fma_f32 v[18:19], v[18:19], v[30:31], v[28:29]
	v_pk_fma_f32 v[20:21], v[20:21], v[24:25], v[22:23]
	global_store_dwordx4 v[6:7], v[18:21], off offset:2048
	s_nop 0
	s_nop 0
	s_nop 0
	s_nop 0
	s_nop 0
	v_lshl_add_u64 v[4:5], v[4:5], 0, s[4:5]
	s_waitcnt vmcnt(7)
	v_mov_b32_e32 v22, v94
	v_mov_b32_e32 v23, v95
	v_mov_b32_e32 v24, v96
	v_mov_b32_e32 v25, v97
	v_mov_b32_e32 v26, v98
	v_mov_b32_e32 v27, v99
	v_mov_b32_e32 v18, v100
	v_mov_b32_e32 v19, v101
	v_mov_b32_e32 v20, v102
	v_mov_b32_e32 v21, v103
	v_lshlrev_b32_e32 v10, 16, v22
	s_nop 0
	v_lshlrev_b32_e32 v12, 16, v24
	s_nop 0
	v_lshlrev_b32_e32 v28, 16, v26
	v_and_b32_e32 v29, 0xffff0000, v26
	v_lshlrev_b32_e32 v26, 16, v27
	v_and_b32_e32 v27, 0xffff0000, v27
	v_and_b32_e32 v13, 0xffff0000, v24
	v_lshlrev_b32_e32 v24, 16, v25
	v_and_b32_e32 v25, 0xffff0000, v25
	v_pk_mul_f32 v[28:29], v[8:9], v[28:29] op_sel_hi:[0,1]
	v_pk_mul_f32 v[26:27], v[8:9], v[26:27] op_sel_hi:[0,1]
	v_and_b32_e32 v11, 0xffff0000, v22
	v_lshlrev_b32_e32 v22, 16, v23
	v_and_b32_e32 v23, 0xffff0000, v23
	v_pk_fma_f32 v[12:13], v[0:1], v[12:13], v[28:29] op_sel_hi:[0,1,1]
	v_pk_fma_f32 v[24:25], v[0:1], v[24:25], v[26:27] op_sel_hi:[0,1,1]
	s_nop 0
	v_pk_fma_f32 v[10:11], v[18:19], v[12:13], v[10:11]
	v_pk_fma_f32 v[12:13], v[20:21], v[24:25], v[22:23]
	global_store_dwordx4 v[6:7], v[10:13], off offset:3072
	v_lshl_add_u64 v[6:7], v[6:7], 0, s[8:9]
	s_cbranch_scc1 .LBB0_2785
